# v79: v78 + gdn_gb LDS operand rows written with the two middle 8-byte pieces of each 32-byte group exchanged (ds_write2_b64) so fragments are read with one conflict-free ds_read_b128 instead of ds_rea
# baseline (speedup 1.0000x reference)
.LBB0_1633:
	v_mfma_f32_32x32x16_bf16 v[52:67], v[164:167], v[100:103], v[52:67]
	s_lshl_b32 s10, s50, 4
	s_bitcmp1_b32 s47, 0
	v_and_b32_e32 v2, 31, v68
	v_ashrrev_i32_e32 v177, 5, v68
	v_mul_u32_u24_e32 v68, 0x110, v2
	v_lshlrev_b32_e32 v168, 4, v177
	v_mfma_f32_32x32x16_bf16 v[36:51], v[178:181], v[100:103], v[36:51]
	s_cselect_b32 s11, 0x11c00, 0
	v_add_u32_e32 v178, s11, v1
	ds_read_b32 v234, v178 offset:62976
	v_add3_u32 v169, v178, v68, v168
	v_add_u32_e32 v237, 0x2000, v169
	ds_read_b128 v[88:91], v237 offset:512
	v_mfma_f32_32x32x16_bf16 v[20:35], v[190:193], v[100:103], v[20:35]
	ds_read_b128 v[92:95], v237 offset:544
	ds_read_b128 v[96:99], v237 offset:576
	ds_read_b128 v[116:119], v237 offset:608
	ds_read_b128 v[68:71], v169
	s_nop 0
	v_cvt_pk_bf16_f32 v160, v36, v37
	v_cvt_pk_bf16_f32 v161, v38, v39
	v_mfma_f32_32x32x16_bf16 v[4:19], v[194:197], v[100:103], v[4:19]
	v_cvt_pk_bf16_f32 v162, v40, v41
	v_cvt_pk_bf16_f32 v163, v42, v43
	v_cvt_pk_bf16_f32 v164, v44, v45
	v_cvt_pk_bf16_f32 v165, v46, v47
	v_cvt_pk_bf16_f32 v166, v48, v49
	v_cvt_pk_bf16_f32 v167, v50, v51
	v_cvt_pk_bf16_f32 v84, v52, v53
	v_cvt_pk_bf16_f32 v85, v54, v55
	v_cvt_pk_bf16_f32 v86, v56, v57
	v_cvt_pk_bf16_f32 v87, v58, v59
	s_waitcnt lgkmcnt(4)
	s_nop 0
	v_mfma_f32_32x32x16_bf16 v[100:115], v[88:91], v[84:87], 0
	ds_read_b128 v[72:75], v169 offset:32
	ds_read_b128 v[76:79], v169 offset:64
	ds_read_b128 v[80:83], v169 offset:96
	ds_read_b128 v[184:187], v237 offset:640
	v_cvt_pk_bf16_f32 v156, v60, v61
	v_cvt_pk_bf16_f32 v157, v62, v63
	v_cvt_pk_bf16_f32 v158, v64, v65
	v_cvt_pk_bf16_f32 v159, v66, v67
	s_waitcnt lgkmcnt(7)
	s_nop 0
	v_mfma_f32_32x32x16_bf16 v[100:115], v[92:95], v[156:159], v[100:115]
	v_cvt_pk_bf16_f32 v144, v20, v21
	v_cvt_pk_bf16_f32 v145, v22, v23
	v_cvt_pk_bf16_f32 v146, v24, v25
	v_cvt_pk_bf16_f32 v147, v26, v27
	ds_read_b128 v[188:191], v237 offset:672
	v_cvt_pk_bf16_f32 v152, v28, v29
	s_waitcnt lgkmcnt(7)
	v_mfma_f32_32x32x16_bf16 v[100:115], v[96:99], v[160:163], v[100:115]
	v_cvt_pk_bf16_f32 v153, v30, v31
	v_cvt_pk_bf16_f32 v154, v32, v33
	v_cvt_pk_bf16_f32 v155, v34, v35
	ds_read_b128 v[196:199], v237 offset:704
	v_cvt_pk_bf16_f32 v148, v4, v5
	v_cvt_pk_bf16_f32 v149, v6, v7
	s_waitcnt lgkmcnt(7)
	v_mfma_f32_32x32x16_bf16 v[100:115], v[116:119], v[164:167], v[100:115]
	v_cvt_pk_bf16_f32 v150, v8, v9
	v_cvt_pk_bf16_f32 v151, v10, v11
	ds_read_b128 v[204:207], v237 offset:736
	v_cvt_pk_bf16_f32 v140, v12, v13
	v_cvt_pk_bf16_f32 v141, v14, v15
	v_cvt_pk_bf16_f32 v142, v16, v17
	s_waitcnt lgkmcnt(7)
	v_mfma_f32_32x32x16_bf16 v[116:131], v[68:71], v[84:87], 0
	v_cvt_pk_bf16_f32 v143, v18, v19
	ds_read_b128 v[170:173], v169 offset:128
	ds_read_b128 v[180:183], v169 offset:160
	ds_read_b128 v[192:195], v169 offset:192
	ds_read_b128 v[200:203], v169 offset:224
	v_add_u32_e32 v239, 0x6000, v169
	s_waitcnt lgkmcnt(10)
	v_mfma_f32_32x32x16_bf16 v[116:131], v[72:75], v[156:159], v[116:131]
	ds_read_b128 v[68:71], v239 offset:1536
	ds_read_b128 v[92:95], v239 offset:1568
	ds_read_b128 v[96:99], v239 offset:1600
	ds_read_b128 v[220:223], v239 offset:1632
	v_add_u32_e32 v238, 0x4000, v169
	ds_read_b128 v[88:91], v238 offset:1024
	s_waitcnt lgkmcnt(14)
	v_mfma_f32_32x32x16_bf16 v[116:131], v[76:79], v[160:163], v[116:131]
	ds_read_b128 v[208:211], v238 offset:1056
	ds_read_b128 v[212:215], v238 offset:1088
	ds_read_b128 v[216:219], v238 offset:1120
	ds_read_b128 v[224:227], v239 offset:1760
	v_mul_f32_e64 v66, v66, v234
	v_mul_f32_e64 v67, v67, v234
	s_waitcnt lgkmcnt(15)
	v_mfma_f32_32x32x16_bf16 v[116:131], v[80:83], v[164:167], v[116:131]
	v_mul_f32_e64 v64, v64, v234
	v_mul_f32_e64 v65, v65, v234
	v_mul_f32_e64 v62, v62, v234
	v_mul_f32_e64 v63, v63, v234
	v_mul_f32_e64 v60, v60, v234
	v_mul_f32_e64 v61, v61, v234
	v_mfma_f32_32x32x16_bf16 v[100:115], v[184:187], v[144:147], v[100:115]
	ds_read_b128 v[184:187], v239 offset:1664
	v_mul_f32_e64 v58, v58, v234
	v_mul_f32_e64 v59, v59, v234
	v_mul_f32_e64 v56, v56, v234
	v_mul_f32_e64 v57, v57, v234
	v_mul_f32_e64 v54, v54, v234
	v_mfma_f32_32x32x16_bf16 v[100:115], v[188:191], v[152:155], v[100:115]
	ds_read_b128 v[188:191], v239 offset:1696
	v_mul_f32_e64 v55, v55, v234
	v_mul_f32_e64 v52, v52, v234
	v_mul_f32_e64 v53, v53, v234
	v_mul_f32_e64 v50, v50, v234
	v_mul_f32_e64 v51, v51, v234
	s_waitcnt lgkmcnt(15)
	v_mfma_f32_32x32x16_bf16 v[100:115], v[196:199], v[148:151], v[100:115]
	ds_read_b128 v[196:199], v239 offset:1728
	v_mul_f32_e64 v48, v48, v234
	v_mul_f32_e64 v49, v49, v234
	v_mul_f32_e64 v46, v46, v234
	v_mul_f32_e64 v47, v47, v234
	v_mul_f32_e64 v44, v44, v234
	v_mfma_f32_32x32x16_bf16 v[100:115], v[204:207], v[140:143], v[100:115]
	ds_read_b128 v[204:207], v238 offset:1248
	v_mul_f32_e64 v45, v45, v234
	v_mul_f32_e64 v42, v42, v234
	v_mul_f32_e64 v43, v43, v234
	v_mul_f32_e64 v40, v40, v234
	v_mul_f32_e64 v41, v41, v234
	s_waitcnt lgkmcnt(15)
	v_mfma_f32_32x32x16_bf16 v[116:131], v[170:173], v[144:147], v[116:131]
	ds_read_b128 v[170:173], v238 offset:1152
	v_mul_f32_e64 v38, v38, v234
	v_mul_f32_e64 v39, v39, v234
	v_mul_f32_e64 v36, v36, v234
	v_mul_f32_e64 v37, v37, v234
	v_mul_f32_e64 v34, v34, v234
	v_mfma_f32_32x32x16_bf16 v[116:131], v[180:183], v[152:155], v[116:131]
	ds_read_b128 v[180:183], v238 offset:1184
	v_mul_f32_e64 v35, v35, v234
	v_mul_f32_e64 v32, v32, v234
	v_mul_f32_e64 v33, v33, v234
	v_mul_f32_e64 v30, v30, v234
	v_mul_f32_e64 v31, v31, v234
	s_waitcnt lgkmcnt(15)
	v_mfma_f32_32x32x16_bf16 v[116:131], v[192:195], v[148:151], v[116:131]
	ds_read_b128 v[192:195], v238 offset:1216
	v_mul_f32_e64 v28, v28, v234
	v_mul_f32_e64 v29, v29, v234
	v_mul_f32_e64 v26, v26, v234
	v_mul_f32_e64 v27, v27, v234
	v_mul_f32_e64 v24, v24, v234
	v_mfma_f32_32x32x16_bf16 v[116:131], v[200:203], v[140:143], v[116:131]
	v_mul_f32_e64 v25, v25, v234
	v_mul_f32_e64 v22, v22, v234
	v_mul_f32_e64 v23, v23, v234
	v_mul_f32_e64 v20, v20, v234
	v_mul_f32_e64 v21, v21, v234
	v_mul_f32_e64 v18, v18, v234
	s_waitcnt lgkmcnt(15)
	v_mfma_f32_32x32x16_bf16 v[68:83], v[84:87], v[68:71], 0
	v_mul_f32_e64 v19, v19, v234
	v_mul_f32_e64 v16, v16, v234
	v_mul_f32_e64 v17, v17, v234
	v_mul_f32_e64 v14, v14, v234
	v_mul_f32_e64 v15, v15, v234
	v_mul_f32_e64 v12, v12, v234
	s_waitcnt lgkmcnt(14)
	v_mfma_f32_32x32x16_bf16 v[68:83], v[156:159], v[92:95], v[68:83]
	v_mul_f32_e64 v13, v13, v234
	v_mul_f32_e64 v10, v10, v234
	v_mul_f32_e64 v11, v11, v234
	v_mul_f32_e64 v8, v8, v234
	v_mul_f32_e64 v9, v9, v234
	v_mul_f32_e64 v6, v6, v234
	s_waitcnt lgkmcnt(13)
	v_mfma_f32_32x32x16_bf16 v[68:83], v[160:163], v[96:99], v[68:83]
	v_mul_f32_e64 v7, v7, v234
	v_mul_f32_e64 v4, v4, v234
	v_mul_f32_e64 v5, v5, v234
	s_or_b32 s10, s10, s42
	s_ashr_i32 s11, s10, 31
	s_lshl_b64 s[10:11], s[10:11], 14
	s_waitcnt lgkmcnt(12)
	v_mfma_f32_32x32x16_bf16 v[68:83], v[164:167], v[220:223], v[68:83]
	s_add_u32 s10, s26, s10
	s_addc_u32 s11, s27, s11
	s_add_u32 s10, s10, s0
	s_addc_u32 s11, s11, s1
	s_add_u32 s10, s10, s0
	s_addc_u32 s11, s11, s1
	s_waitcnt lgkmcnt(11)
	v_mfma_f32_32x32x16_bf16 v[84:99], v[84:87], v[88:91], 0
	v_lshlrev_b32_e32 v235, 4, v177
	v_lshl_add_u32 v235, v2, 8, v235
	v_add_u32_e32 v236, 0x2000, v235
	s_waitcnt lgkmcnt(10)
	v_mfma_f32_32x32x16_bf16 v[84:99], v[156:159], v[208:211], v[84:99]
	v_lshlrev_b32_e32 v156, 4, v177
	v_add3_u32 v156, v178, s41, v156
	v_mad_u32_u24 v158, v2, s33, v156
	ds_read_b128 v[200:203], v158 offset:63488
	ds_read_b128 v[208:211], v158 offset:63520
	v_mov_b32_e32 v159, 0x1200
	s_waitcnt lgkmcnt(11)
	v_mfma_f32_32x32x16_bf16 v[84:99], v[160:163], v[212:215], v[84:99]
	v_mad_u32_u24 v159, v2, s33, v159
	v_add_u32_e32 v156, v156, v159
	ds_read_b128 v[212:215], v156 offset:63488
	ds_read_b128 v[220:223], v156 offset:63520
	v_add3_u32 v232, v178, v159, v168
	v_mul_u32_u24_e32 v157, 0x90, v2
	s_waitcnt lgkmcnt(12)
	v_mfma_f32_32x32x16_bf16 v[84:99], v[164:167], v[216:219], v[84:99]
	v_add3_u32 v179, v178, v157, v168
	v_add_u32_e32 v156, 0xd000, v179
	ds_read_b128 v[216:219], v156 offset:32
	ds_read_b128 v[228:231], v156 offset:96
	v_add_u32_e32 v157, 0xd000, v232
	ds_read_b128 v[164:167], v157 offset:32
	s_waitcnt lgkmcnt(9)
	v_mfma_f32_32x32x16_bf16 v[84:99], v[144:147], v[170:173], v[84:99]
	ds_read_b128 v[168:171], v157
	ds_read_b128 v[160:163], v157 offset:64
	s_waitcnt lgkmcnt(10)
	v_mfma_f32_32x32x16_bf16 v[84:99], v[152:155], v[180:183], v[84:99]
	ds_read_b128 v[180:183], v156
	s_waitcnt lgkmcnt(10)
	v_mfma_f32_32x32x16_bf16 v[84:99], v[148:151], v[192:195], v[84:99]
	ds_read_b128 v[192:195], v156 offset:64
	ds_read_b128 v[156:159], v157 offset:96
	v_mfma_f32_32x32x16_bf16 v[84:99], v[140:143], v[204:207], v[84:99]
	s_waitcnt lgkmcnt(11)
	v_mfma_f32_32x32x16_bf16 v[116:131], v[200:203], v[132:135], v[116:131]
	s_waitcnt lgkmcnt(9)
	v_mfma_f32_32x32x16_bf16 v[100:115], v[212:215], v[132:135], v[100:115]
	v_mfma_f32_32x32x16_bf16 v[116:131], v[208:211], v[136:139], v[116:131]
	s_waitcnt lgkmcnt(8)
	v_mfma_f32_32x32x16_bf16 v[100:115], v[220:223], v[136:139], v[100:115]
	v_mfma_f32_32x32x16_bf16 v[68:83], v[144:147], v[184:187], v[68:83]
	v_add_u32_e32 v184, 0x8800, v179
	v_add_u32_e32 v185, 0x8800, v232
	v_mfma_f32_32x32x16_bf16 v[68:83], v[152:155], v[188:191], v[68:83]
	v_add_u32_e32 v190, 0xa800, v179
	v_mfma_f32_32x32x16_bf16 v[68:83], v[148:151], v[196:199], v[68:83]
	v_add_u32_e32 v196, 0xb800, v179
	ds_read_b128 v[144:147], v196 offset:1536
	ds_read_b128 v[148:151], v190 offset:1056
	ds_read_b128 v[152:155], v196 offset:1568
	v_cvt_pk_bf16_f32 v172, v116, v117
	v_cvt_pk_bf16_f32 v173, v118, v119
	v_mfma_f32_32x32x16_bf16 v[68:83], v[140:143], v[224:227], v[68:83]
	v_cvt_pk_bf16_f32 v118, v104, v105
	v_cvt_pk_bf16_f32 v119, v106, v107
	v_cvt_pk_bf16_f32 v174, v120, v121
	v_cvt_pk_bf16_f32 v120, v124, v125
	v_cvt_pk_bf16_f32 v121, v126, v127
	v_cvt_pk_bf16_f32 v175, v122, v123
	s_waitcnt lgkmcnt(5)
	s_nop 0
	v_mfma_f32_32x32x16_bf16 v[84:99], v[172:175], v[180:183], v[84:99]
	v_cvt_pk_bf16_f32 v122, v128, v129
	v_cvt_pk_bf16_f32 v123, v130, v131
	ds_read_b128 v[124:127], v185
	v_cvt_pk_bf16_f32 v116, v100, v101
	v_cvt_pk_bf16_f32 v100, v108, v109
	v_cvt_pk_bf16_f32 v101, v110, v111
	v_mfma_f32_32x32x16_bf16 v[84:99], v[120:123], v[216:219], v[84:99]
	ds_read_b128 v[108:111], v184
	v_cvt_pk_bf16_f32 v117, v102, v103
	v_cvt_pk_bf16_f32 v102, v112, v113
	v_cvt_pk_bf16_f32 v103, v114, v115
	ds_read_b128 v[128:131], v190 offset:1024
	ds_read_b128 v[104:107], v184 offset:32
	s_waitcnt lgkmcnt(8)
	v_mfma_f32_32x32x16_bf16 v[84:99], v[116:119], v[192:195], v[84:99]
	ds_read_b128 v[112:115], v185 offset:32
	ds_read_b128 v[140:143], v184 offset:64
	ds_read_b128 v[178:181], v185 offset:96
	ds_read_b128 v[186:189], v196 offset:1600
	ds_read_b128 v[194:197], v196 offset:1632
	v_mfma_f32_32x32x16_bf16 v[84:99], v[100:103], v[228:231], v[84:99]
	v_mfma_f32_32x32x16_bf16 v[68:83], v[172:175], v[168:171], v[68:83]
	ds_read_b128 v[168:171], v185 offset:64
	v_mfma_f32_32x32x16_bf16 v[68:83], v[120:123], v[164:167], v[68:83]
	ds_read_b128 v[164:167], v184 offset:96
	ds_read_b128 v[182:185], v190 offset:1088
	ds_read_b128 v[190:193], v190 offset:1120
	v_mfma_f32_32x32x16_bf16 v[68:83], v[116:119], v[160:163], v[68:83]
	s_waitcnt lgkmcnt(15)
	v_mfma_f32_32x32x16_bf16 v[68:83], v[100:103], v[156:159], v[68:83]
	s_waitcnt lgkmcnt(11)
	v_mfma_f32_32x32x16_bf16 v[52:67], v[108:111], v[172:175], v[52:67]
	v_mfma_f32_32x32x16_bf16 v[36:51], v[124:127], v[172:175], v[36:51]
	s_waitcnt lgkmcnt(10)
	v_mfma_f32_32x32x16_bf16 v[20:35], v[128:131], v[172:175], v[20:35]
	v_cvt_pk_bf16_f32 v84, v84, v85
	v_cvt_pk_bf16_f32 v85, v86, v87
	v_cvt_pk_bf16_f32 v86, v88, v89
	v_cvt_pk_bf16_f32 v87, v90, v91
	v_cvt_pk_bf16_f32 v88, v92, v93
	v_cvt_pk_bf16_f32 v89, v94, v95
	v_mfma_f32_32x32x16_bf16 v[4:19], v[144:147], v[172:175], v[4:19]
	v_cvt_pk_bf16_f32 v90, v96, v97
	v_cvt_pk_bf16_f32 v91, v98, v99
	v_permlane32_swap_b32_e32 v84, v86
	v_permlane32_swap_b32_e32 v85, v87
	v_permlane32_swap_b32_e32 v88, v90
	v_permlane32_swap_b32_e32 v89, v91
	s_waitcnt lgkmcnt(9)
	v_mfma_f32_32x32x16_bf16 v[52:67], v[104:107], v[120:123], v[52:67]
	global_store_dwordx4 v235, v[84:87], s[10:11]
	global_store_dwordx4 v235, v[88:91], s[10:11] offset:32
	v_cvt_pk_bf16_f32 v68, v68, v69
	v_cvt_pk_bf16_f32 v69, v70, v71
	v_cvt_pk_bf16_f32 v70, v72, v73
	v_cvt_pk_bf16_f32 v71, v74, v75
	s_waitcnt lgkmcnt(8)
	v_mfma_f32_32x32x16_bf16 v[36:51], v[112:115], v[120:123], v[36:51]
	v_cvt_pk_bf16_f32 v72, v76, v77
	v_cvt_pk_bf16_f32 v73, v78, v79
	v_cvt_pk_bf16_f32 v74, v80, v81
	v_cvt_pk_bf16_f32 v75, v82, v83
	v_permlane32_swap_b32_e32 v68, v70
	v_permlane32_swap_b32_e32 v69, v71
	v_mfma_f32_32x32x16_bf16 v[20:35], v[148:151], v[120:123], v[20:35]
	v_permlane32_swap_b32_e32 v72, v74
	v_permlane32_swap_b32_e32 v73, v75
	global_store_dwordx4 v236, v[68:71], s[10:11]
	global_store_dwordx4 v236, v[72:75], s[10:11] offset:32
	v_mfma_f32_32x32x16_bf16 v[4:19], v[152:155], v[120:123], v[4:19]
	s_waitcnt lgkmcnt(7)
	v_mfma_f32_32x32x16_bf16 v[52:67], v[140:143], v[116:119], v[52:67]
	s_waitcnt lgkmcnt(3)
	v_mfma_f32_32x32x16_bf16 v[36:51], v[168:171], v[116:119], v[36:51]
	s_waitcnt lgkmcnt(1)
	v_mfma_f32_32x32x16_bf16 v[20:35], v[182:185], v[116:119], v[20:35]
	v_mfma_f32_32x32x16_bf16 v[4:19], v[186:189], v[116:119], v[4:19]
	s_waitcnt lgkmcnt(0)
	s_barrier
	s_add_i32 s43, s43, -1
	s_add_i32 s46, s46, 1
	s_cmp_lg_u32 s43, -1
	s_cbranch_scc0 .LBB0_1638

.LBB0_1639:
	s_lshl_b32 s42, s38, 2
	s_bitset1_b32 s42, 8
	s_cmp_eq_u32 s39, 0
	s_cselect_b64 s[0:1], -1, 0
	s_and_b64 s[8:9], s[0:1], exec
	s_cselect_b32 s8, 0, 3
	s_cselect_b32 s43, 3, 0
	s_or_b32 s8, s42, s8
	s_lshl_b32 s41, s3, 1
	s_lshl_b32 s9, s8, 4
	s_or_b32 s8, s41, s39
	s_or_b32 s52, s8, s9
	s_lshl_b32 s3, s52, 13
	s_lshl_b32 s25, s52, 14
	s_add_u32 s10, s15, s25
	s_addc_u32 s11, s17, 0
	s_add_u32 s46, s13, s25
	s_addc_u32 s47, s14, 0
	s_add_u32 s50, s20, s25
	v_mov_b32_e32 v2, v176
	s_addc_u32 s51, s21, 0
	s_lshl_b32 s9, s35, 11
	v_mov_b32_e32 v72, v176
	s_waitcnt vmcnt(0)
	v_lshl_add_u32 v52, v2, 3, s9
	v_ashrrev_i32_e32 v53, 31, v52
	v_lshlrev_b64 v[12:13], 1, v[52:53]
	v_lshl_add_u64 v[40:41], s[46:47], 0, v[12:13]
	s_add_u32 s46, s18, s3
	v_lshl_add_u64 v[32:33], s[10:11], 0, v[12:13]
	s_addc_u32 s47, s19, 0
	s_lshl_b32 s11, s35, 7
	v_add_u32_e32 v2, s11, v2
	s_lshl_b32 s10, s35, 10
	v_add_u32_e32 v66, 64, v2
	v_subrev_u32_e32 v52, s10, v52
	v_ashrrev_i32_e32 v60, 31, v2
	v_ashrrev_i32_e32 v64, 31, v66
	v_ashrrev_i32_e32 v53, 31, v52
	s_add_u32 s25, s31, s25
	v_lshrrev_b32_e32 v60, 29, v60
	v_lshrrev_b32_e32 v64, 29, v64
	v_lshl_add_u64 v[56:57], v[52:53], 1, s[46:47]
	s_addc_u32 s47, s36, 0
	s_ashr_i32 s3, s2, 31
	v_add_u32_e32 v62, v2, v60
	v_add_u32_e32 v67, v66, v64
	s_lshl_b64 s[2:3], s[2:3], 1
	v_lshlrev_b32_e32 v60, 4, v62
	v_lshlrev_b32_e32 v64, 4, v67
	s_add_u32 s46, s25, s2
	v_and_b32_e32 v60, 0xffffff80, v60
	v_and_b32_e32 v64, 0xffffff80, v64
	s_addc_u32 s47, s47, s3
	v_ashrrev_i32_e32 v61, 31, v60
	v_and_b32_e32 v62, 0x1ffffff8, v62
	v_ashrrev_i32_e32 v65, 31, v64
	s_lshl_b32 s25, s35, 6
	v_lshl_add_u64 v[60:61], v[60:61], 1, s[46:47]
	v_sub_u32_e32 v62, v2, v62
	v_lshl_add_u64 v[64:65], v[64:65], 1, s[46:47]
	v_subrev_u32_e32 v2, s25, v2
	s_mul_hi_u32 s47, s52, 0x300
	s_mulk_i32 s52, 0x300
	v_min_i32_e32 v68, 0xbf, v2
	s_add_u32 s46, s22, s52
	v_ashrrev_i32_e32 v69, 31, v68
	s_addc_u32 s47, s23, s47
	global_load_dwordx4 v[4:7], v[32:33], off
	global_load_dwordx4 v[8:11], v[40:41], off
	v_lshl_add_u64 v[48:49], s[50:51], 0, v[12:13]
	v_lshl_add_u64 v[68:69], v[68:69], 2, s[46:47]
	global_load_dwordx4 v[12:15], v[48:49], off
	global_load_dwordx4 v[16:19], v[32:33], off offset:1024
	global_load_dwordx4 v[20:23], v[40:41], off offset:1024
	global_load_dwordx4 v[24:27], v[48:49], off offset:1024
	global_load_dwordx4 v[28:31], v[32:33], off offset:2048
	s_nop 0
	global_load_dwordx4 v[32:35], v[32:33], off offset:3072
	s_nop 0
	global_load_dwordx4 v[36:39], v[40:41], off offset:2048
	s_nop 0
	global_load_dwordx4 v[40:43], v[40:41], off offset:3072
	s_nop 0
	global_load_dwordx4 v[44:47], v[48:49], off offset:2048
	s_nop 0
	global_load_dwordx4 v[48:51], v[48:49], off offset:3072
	s_nop 0
	global_load_dwordx4 v[52:55], v[56:57], off
	s_nop 0
	global_load_dwordx4 v[56:59], v[56:57], off offset:1024
	v_lshlrev_b32_e32 v62, 3, v62
	global_load_dword v69, v[68:69], off
	v_ashrrev_i32_e32 v63, 31, v62
	v_lshl_add_u64 v[60:61], v[62:63], 1, v[60:61]
	global_load_dwordx4 v[60:63], v[60:61], off
	v_and_b32_e32 v67, 0x1ffffff8, v67
	v_sub_u32_e32 v66, v66, v67
	v_lshlrev_b32_e32 v66, 3, v66
	v_ashrrev_i32_e32 v67, 31, v66
	v_lshl_add_u64 v[64:65], v[66:67], 1, v[64:65]
	global_load_dwordx4 v[64:67], v[64:65], off
	s_lshl_b32 s35, s35, 8
	v_lshlrev_b32_e32 v68, 4, v72
	v_add_u32_e32 v73, s35, v72
	v_and_b32_e32 v2, 0xf0, v68
	v_add_u32_e32 v2, v1, v2
	v_lshrrev_b32_e32 v70, 4, v73
	v_and_b32_e32 v68, 0x70, v68
	v_mad_u64_u32 v[70:71], s[46:47], v70, s30, v[2:3]
	v_add_u32_e32 v68, v1, v68
	v_mov_b32_e32 v124, v176
	v_add_u32_e32 v132, 0x16000, v1
	v_add_u32_e32 v133, 0x1a400, v1
	v_add_u32_e32 v134, 0x1ec00, v1
	s_waitcnt vmcnt(16)
	v_mbcnt_lo_u32_b32 v240, -1, 0
	v_mbcnt_hi_u32_b32 v240, -1, v240
	v_and_b32_e32 v240, 1, v240
	v_lshlrev_b32_e32 v240, 3, v240
	v_sub_u32_e32 v240, 0, v240
	v_add_u32_e32 v241, v70, v240
	ds_write2_b64 v241, v[4:5], v[6:7] offset1:2
	s_waitcnt vmcnt(15)
	v_add_u32_e32 v242, 0x4400, v70
	v_add_u32_e32 v242, v242, v240
	ds_write2_b64 v242, v[8:9], v[10:11] offset1:2
	v_lshrrev_b32_e32 v4, 3, v73
	v_add_u32_e32 v6, 64, v73
	v_add_u32_e32 v135, 0x21400, v1
	v_add_u32_e32 v136, 0x21000, v1
	s_mov_b32 s40, 0
	s_waitcnt vmcnt(2)
	v_mad_u64_u32 v[4:5], s[46:47], v4, s33, v[68:69]
	v_add_u32_e32 v241, 0x8800, v4
	v_add_u32_e32 v241, v241, v240
	ds_write2_b64 v241, v[12:13], v[14:15] offset1:2
	v_lshrrev_b32_e32 v4, 4, v6
	v_mad_u64_u32 v[4:5], s[46:47], v4, s30, v[2:3]
	v_add_u32_e32 v242, v4, v240
	ds_write2_b64 v242, v[16:17], v[18:19] offset1:2
	v_add_u32_e32 v241, 0x4400, v4
	v_add_u32_e32 v241, v241, v240
	ds_write2_b64 v241, v[20:21], v[22:23] offset1:2
	v_lshrrev_b32_e32 v4, 3, v6
	v_mad_u64_u32 v[4:5], s[46:47], v4, s33, v[68:69]
	v_add_u32_e32 v6, 0x80, v73
	v_add_u32_e32 v242, 0x8800, v4
	v_add_u32_e32 v242, v242, v240
	ds_write2_b64 v242, v[24:25], v[26:27] offset1:2
	v_lshrrev_b32_e32 v4, 4, v6
	v_mad_u64_u32 v[4:5], s[46:47], v4, s30, v[2:3]
	v_add_u32_e32 v241, v4, v240
	ds_write2_b64 v241, v[28:29], v[30:31] offset1:2
	v_add_u32_e32 v242, 0x4400, v4
	v_add_u32_e32 v242, v242, v240
	ds_write2_b64 v242, v[36:37], v[38:39] offset1:2
	v_lshrrev_b32_e32 v4, 3, v6
	v_mad_u64_u32 v[4:5], s[46:47], v4, s33, v[68:69]
	v_add_u32_e32 v6, 0xc0, v73
	v_add_u32_e32 v241, 0x8800, v4
	v_add_u32_e32 v241, v241, v240
	ds_write2_b64 v241, v[44:45], v[46:47] offset1:2
	v_lshrrev_b32_e32 v4, 4, v6
	v_mad_u64_u32 v[4:5], s[46:47], v4, s30, v[2:3]
	v_lshrrev_b32_e32 v2, 3, v6
	v_add_u32_e32 v242, v4, v240
	ds_write2_b64 v242, v[32:33], v[34:35] offset1:2
	v_add_u32_e32 v241, 0x4400, v4
	v_add_u32_e32 v241, v241, v240
	ds_write2_b64 v241, v[40:41], v[42:43] offset1:2
	v_mad_u64_u32 v[4:5], s[46:47], v2, s33, v[68:69]
	v_add_u32_e32 v2, s11, v72
	v_add_u32_e32 v242, 0x8800, v4
	v_add_u32_e32 v242, v242, v240
	ds_write2_b64 v242, v[48:49], v[50:51] offset1:2
	v_lshrrev_b32_e32 v4, 3, v2
	v_mad_u64_u32 v[4:5], s[46:47], v4, s33, v[68:69]
	v_add_u32_e32 v6, 64, v2
	v_add_u32_e32 v241, 0xd000, v4
	v_add_u32_e32 v241, v241, v240
	ds_write2_b64 v241, v[52:53], v[54:55] offset1:2
	v_lshrrev_b32_e32 v4, 3, v6
	v_mad_u64_u32 v[4:5], s[46:47], v4, s33, v[68:69]
	v_add_u32_e32 v242, 0xd000, v4
	v_add_u32_e32 v242, v242, v240
	ds_write2_b64 v242, v[56:57], v[58:59] offset1:2
	v_ashrrev_i32_e32 v4, 31, v2
	v_lshrrev_b32_e32 v4, 29, v4
	v_add_u32_e32 v4, v2, v4
	v_lshrrev_b32_e32 v5, 3, v4
	v_and_b32_e32 v4, 0xffffff8, v4
	v_sub_u32_e32 v4, v2, v4
	v_mul_lo_u32 v5, v5, s33
	v_lshlrev_b32_e32 v4, 4, v4
	v_add3_u32 v4, v1, v5, v4
	s_waitcnt vmcnt(1)
	ds_write_b128 v4, v[60:63] offset:63488
	v_ashrrev_i32_e32 v4, 31, v6
	s_or_b32 s46, s39, s42
	v_lshrrev_b32_e32 v4, 29, v4
	s_lshl_b32 s46, s46, 4
	v_add_u32_e32 v4, v6, v4
	s_or_b32 s46, s46, s8
	v_lshrrev_b32_e32 v5, 3, v4
	v_and_b32_e32 v4, 0xffffff8, v4
	s_add_i32 s80, s46, 16
	v_sub_u32_e32 v4, v6, v4
	v_subrev_u32_e32 v2, s25, v2
	s_lshl_b64 s[46:47], s[80:81], 13
	s_lshl_b64 s[50:51], s[80:81], 14
	v_mul_lo_u32 v5, v5, s33
	v_lshlrev_b32_e32 v4, 4, v4
	v_min_i32_e32 v2, 0xbf, v2
	s_add_u32 s52, s15, s50
	v_add3_u32 v4, v1, v5, v4
	v_lshl_add_u32 v2, v2, 2, v1
	s_addc_u32 s53, s17, s51
	s_waitcnt vmcnt(0)
	ds_write_b128 v4, v[64:67] offset:63488
	ds_write_b32 v2, v69 offset:62464
	v_mov_b32_e32 v2, v176
	s_add_u32 s54, s13, s50
	s_addc_u32 s55, s14, s51
	v_lshl_add_u32 v52, v2, 3, s9
	s_add_u32 s56, s20, s50
	v_ashrrev_i32_e32 v53, 31, v52
	s_addc_u32 s57, s21, s51
	v_lshlrev_b64 v[4:5], 1, v[52:53]
	v_lshl_add_u64 v[32:33], s[52:53], 0, v[4:5]
	v_lshl_add_u64 v[40:41], s[54:55], 0, v[4:5]
	v_lshl_add_u64 v[48:49], s[56:57], 0, v[4:5]
	global_load_dwordx4 v[4:7], v[32:33], off
	global_load_dwordx4 v[8:11], v[32:33], off offset:1024
	global_load_dwordx4 v[12:15], v[40:41], off
	global_load_dwordx4 v[16:19], v[40:41], off offset:1024
	global_load_dwordx4 v[20:23], v[48:49], off
	global_load_dwordx4 v[24:27], v[48:49], off offset:1024
	global_load_dwordx4 v[28:31], v[32:33], off offset:2048
	s_nop 0
	global_load_dwordx4 v[32:35], v[32:33], off offset:3072
	s_nop 0
	global_load_dwordx4 v[36:39], v[40:41], off offset:2048
	s_nop 0
	global_load_dwordx4 v[40:43], v[40:41], off offset:3072
	s_nop 0
	global_load_dwordx4 v[44:47], v[48:49], off offset:2048
	s_nop 0
	global_load_dwordx4 v[48:51], v[48:49], off offset:3072
	v_add_u32_e32 v2, s11, v2
	s_add_u32 s46, s18, s46
	v_subrev_u32_e32 v52, s10, v52
	v_ashrrev_i32_e32 v60, 31, v2
	s_addc_u32 s47, s19, s47
	v_ashrrev_i32_e32 v53, 31, v52
	v_lshrrev_b32_e32 v60, 29, v60
	v_lshl_add_u64 v[56:57], v[52:53], 1, s[46:47]
	s_add_u32 s46, s31, s50
	v_add_u32_e32 v62, v2, v60
	s_addc_u32 s47, s36, s51
	v_lshlrev_b32_e32 v60, 4, v62
	v_and_b32_e32 v62, 0x1ffffff8, v62
	s_add_u32 s46, s46, s2
	v_and_b32_e32 v60, 0xffffff80, v60
	v_sub_u32_e32 v62, v2, v62
	global_load_dwordx4 v[52:55], v[56:57], off
	s_nop 0
	global_load_dwordx4 v[56:59], v[56:57], off offset:1024
	s_addc_u32 s47, s47, s3
	v_ashrrev_i32_e32 v61, 31, v60
	v_lshlrev_b32_e32 v62, 3, v62
	v_lshl_add_u64 v[60:61], v[60:61], 1, s[46:47]
	v_ashrrev_i32_e32 v63, 31, v62
	v_add_u32_e32 v64, 64, v2
	v_lshl_add_u64 v[60:61], v[62:63], 1, v[60:61]
	v_ashrrev_i32_e32 v62, 31, v64
	v_lshrrev_b32_e32 v62, 29, v62
	v_add_u32_e32 v65, v64, v62
	v_lshlrev_b32_e32 v62, 4, v65
	v_and_b32_e32 v65, 0x1ffffff8, v65
	v_and_b32_e32 v62, 0xffffff80, v62
	v_sub_u32_e32 v64, v64, v65
	v_ashrrev_i32_e32 v63, 31, v62
	v_lshlrev_b32_e32 v64, 3, v64
	v_lshl_add_u64 v[62:63], v[62:63], 1, s[46:47]
	v_ashrrev_i32_e32 v65, 31, v64
	v_lshl_add_u64 v[64:65], v[64:65], 1, v[62:63]
	global_load_dwordx4 v[60:63], v[60:61], off
	s_nop 0
	global_load_dwordx4 v[64:67], v[64:65], off
	v_subrev_u32_e32 v2, s25, v2
	s_mul_i32 s46, s80, 0x300
	v_min_i32_e32 v68, 0xbf, v2
	s_mul_hi_u32 s47, s80, 0x300
	s_add_u32 s46, s22, s46
	v_ashrrev_i32_e32 v69, 31, v68
	s_addc_u32 s47, s23, s47
	v_lshl_add_u64 v[68:69], v[68:69], 2, s[46:47]
	global_load_dword v137, v[68:69], off
	s_lshl_b32 s38, s38, 6
	s_sub_i32 s46, s42, s39
	s_add_u32 s2, s31, s2
	s_addc_u32 s3, s36, s3
	s_or_b32 s42, s42, s43
	s_lshl_b32 s43, s46, 4
	s_or_b32 s43, s43, s39
	s_or_b32 s43, s43, s41
	s_add_i32 s80, s43, 32
	s_lshl_b64 s[46:47], s[80:81], 13
	s_lshl_b64 s[50:51], s[80:81], 14
	s_add_u32 s52, s15, s50
	s_addc_u32 s53, s17, s51
	s_add_u32 s54, s13, s50
	s_waitcnt lgkmcnt(0)
	s_barrier
	s_addc_u32 s55, s14, s51
	v_add_u32_e32 v138, s11, v124
	s_add_u32 s56, s20, s50
	v_lshl_add_u32 v80, v124, 3, s9
	v_ashrrev_i32_e32 v124, 31, v138
	s_addc_u32 s57, s21, s51
	v_ashrrev_i32_e32 v81, 31, v80
	v_lshrrev_b32_e32 v124, 29, v124
	v_lshlrev_b64 v[68:69], 1, v[80:81]
	s_add_u32 s46, s18, s46
	v_subrev_u32_e32 v80, s10, v80
	v_add_u32_e32 v126, v138, v124
	s_addc_u32 s47, s19, s47
	v_ashrrev_i32_e32 v81, 31, v80
	v_lshlrev_b32_e32 v124, 4, v126
	v_and_b32_e32 v126, 0x1ffffff8, v126
	v_lshl_add_u64 v[80:81], v[80:81], 1, s[46:47]
	s_add_u32 s46, s2, s50
	v_and_b32_e32 v124, 0xffffff80, v124
	v_sub_u32_e32 v126, v138, v126
	s_addc_u32 s47, s3, s51
	v_ashrrev_i32_e32 v125, 31, v124
	v_lshlrev_b32_e32 v126, 3, v126
	v_lshl_add_u64 v[124:125], v[124:125], 1, s[46:47]
	v_ashrrev_i32_e32 v127, 31, v126
	v_add_u32_e32 v128, 64, v138
	v_lshl_add_u64 v[124:125], v[126:127], 1, v[124:125]
	v_ashrrev_i32_e32 v126, 31, v128
	v_lshrrev_b32_e32 v126, 29, v126
	v_add_u32_e32 v129, v128, v126
	v_lshlrev_b32_e32 v126, 4, v129
	v_and_b32_e32 v126, 0xffffff80, v126
	v_ashrrev_i32_e32 v127, 31, v126
	v_and_b32_e32 v129, 0x1ffffff8, v129
	v_lshl_add_u64 v[126:127], v[126:127], 1, s[46:47]
	v_sub_u32_e32 v128, v128, v129
	v_subrev_u32_e32 v138, s25, v138
	s_mul_i32 s46, s80, 0x300
	v_lshlrev_b32_e32 v128, 3, v128
	v_min_i32_e32 v138, 0xbf, v138
	s_mul_hi_u32 s43, s80, 0x300
	s_add_u32 s46, s22, s46
	v_ashrrev_i32_e32 v129, 31, v128
	v_ashrrev_i32_e32 v139, 31, v138
	s_addc_u32 s47, s23, s43
	v_lshl_add_u64 v[70:71], s[52:53], 0, v[68:69]
	v_lshl_add_u64 v[72:73], s[54:55], 0, v[68:69]
	v_lshl_add_u64 v[74:75], s[56:57], 0, v[68:69]
	v_lshl_add_u64 v[126:127], v[128:129], 1, v[126:127]
	v_lshl_add_u64 v[138:139], v[138:139], 2, s[46:47]
	global_load_dwordx4 v[112:115], v[70:71], off
	global_load_dwordx4 v[96:99], v[70:71], off offset:1024
	global_load_dwordx4 v[120:123], v[72:73], off
	global_load_dwordx4 v[108:111], v[72:73], off offset:1024
	global_load_dwordx4 v[116:119], v[74:75], off
	global_load_dwordx4 v[100:103], v[74:75], off offset:1024
	global_load_dwordx4 v[84:87], v[70:71], off offset:2048
	s_nop 0
	global_load_dwordx4 v[68:71], v[70:71], off offset:3072
	s_nop 0
	global_load_dwordx4 v[104:107], v[72:73], off offset:2048
	global_load_dwordx4 v[76:79], v[72:73], off offset:3072
	global_load_dwordx4 v[92:95], v[74:75], off offset:2048
	s_nop 0
	global_load_dwordx4 v[72:75], v[74:75], off offset:3072
	s_nop 0
	global_load_dwordx4 v[88:91], v[80:81], off
	s_nop 0
	global_load_dwordx4 v[80:83], v[80:81], off offset:1024
	s_nop 0
	global_load_dwordx4 v[128:131], v[124:125], off
	s_nop 0
	global_load_dwordx4 v[124:127], v[126:127], off
	v_add_u32_e32 v2, 0x11c00, v1
	global_load_dword v141, v[138:139], off
	v_mov_b32_e32 v139, v176
	s_lshl_b32 s42, s42, 4
	v_add_u32_e32 v140, s35, v139
	v_lshlrev_b32_e32 v138, 4, v139
	v_and_b32_e32 v142, 0xf0, v138
	v_lshrrev_b32_e32 v145, 4, v140
	v_add_u32_e32 v143, v2, v142
	v_mul_lo_u32 v145, v145, s30
	v_add_u32_e32 v142, v132, v142
	v_add_u32_e32 v146, v143, v145
	v_and_b32_e32 v144, 0x70, v138
	s_waitcnt vmcnt(33)
	v_mbcnt_lo_u32_b32 v240, -1, 0
	v_mbcnt_hi_u32_b32 v240, -1, v240
	v_and_b32_e32 v240, 1, v240
	v_lshlrev_b32_e32 v240, 3, v240
	v_sub_u32_e32 v240, 0, v240
	v_add_u32_e32 v241, v146, v240
	ds_write2_b64 v241, v[4:5], v[6:7] offset1:2
	v_add_u32_e32 v4, v142, v145
	v_add_u32_e32 v138, v133, v144
	s_waitcnt vmcnt(31)
	v_add_u32_e32 v242, v4, v240
	ds_write2_b64 v242, v[12:13], v[14:15] offset1:2
	v_lshrrev_b32_e32 v4, 3, v140
	v_mad_u64_u32 v[4:5], s[46:47], v4, s33, v[138:139]
	s_waitcnt vmcnt(29)
	v_add_u32_e32 v241, v4, v240
	ds_write2_b64 v241, v[20:21], v[22:23] offset1:2
	v_add_u32_e32 v4, 64, v140
	v_lshrrev_b32_e32 v5, 4, v4
	v_mul_lo_u32 v5, v5, s30
	v_add_u32_e32 v6, v143, v5
	v_add_u32_e32 v5, v142, v5
	v_lshrrev_b32_e32 v4, 3, v4
	v_add_u32_e32 v242, v5, v240
	ds_write2_b64 v242, v[16:17], v[18:19] offset1:2
	v_mad_u64_u32 v[4:5], s[46:47], v4, s33, v[138:139]
	v_add_u32_e32 v241, v6, v240
	ds_write2_b64 v241, v[8:9], v[10:11] offset1:2
	s_waitcnt vmcnt(28)
	v_add_u32_e32 v242, v4, v240
	ds_write2_b64 v242, v[24:25], v[26:27] offset1:2
	v_add_u32_e32 v4, 0x80, v140
	v_lshrrev_b32_e32 v5, 4, v4
	v_mul_lo_u32 v5, v5, s30
	v_add_u32_e32 v6, v143, v5
	v_add_u32_e32 v5, v142, v5
	v_lshrrev_b32_e32 v4, 3, v4
	s_waitcnt vmcnt(25)
	v_add_u32_e32 v241, v5, v240
	ds_write2_b64 v241, v[36:37], v[38:39] offset1:2
	v_mad_u64_u32 v[4:5], s[46:47], v4, s33, v[138:139]
	v_add_u32_e32 v242, v6, v240
	ds_write2_b64 v242, v[28:29], v[30:31] offset1:2
	s_waitcnt vmcnt(23)
	v_add_u32_e32 v241, v4, v240
	ds_write2_b64 v241, v[44:45], v[46:47] offset1:2
	v_add_u32_e32 v4, 0xc0, v140
	v_lshrrev_b32_e32 v5, 4, v4
	v_mul_lo_u32 v5, v5, s30
	v_add_u32_e32 v6, v143, v5
	v_add_u32_e32 v5, v142, v5
	v_lshrrev_b32_e32 v4, 3, v4
	v_add_u32_e32 v242, v5, v240
	ds_write2_b64 v242, v[40:41], v[42:43] offset1:2
	v_mad_u64_u32 v[4:5], s[46:47], v4, s33, v[138:139]
	v_add_u32_e32 v8, s11, v139
	v_add_u32_e32 v241, v6, v240
	ds_write2_b64 v241, v[32:33], v[34:35] offset1:2
	s_waitcnt vmcnt(22)
	v_add_u32_e32 v242, v4, v240
	ds_write2_b64 v242, v[48:49], v[50:51] offset1:2
	v_add_u32_e32 v4, v134, v144
	v_lshrrev_b32_e32 v5, 3, v8
	v_mad_u64_u32 v[6:7], s[46:47], v5, s33, v[4:5]
	s_waitcnt vmcnt(21)
	v_add_u32_e32 v241, v6, v240
	ds_write2_b64 v241, v[52:53], v[54:55] offset1:2
	v_add_u32_e32 v6, 64, v8
	v_lshrrev_b32_e32 v5, 3, v6
	v_mad_u64_u32 v[4:5], s[46:47], v5, s33, v[4:5]
	s_waitcnt vmcnt(20)
	v_add_u32_e32 v242, v4, v240
	ds_write2_b64 v242, v[56:57], v[58:59] offset1:2
	v_ashrrev_i32_e32 v4, 31, v8
	v_lshrrev_b32_e32 v4, 29, v4
	v_add_u32_e32 v4, v8, v4
	v_lshrrev_b32_e32 v5, 3, v4
	v_and_b32_e32 v4, 0xffffff8, v4
	v_sub_u32_e32 v4, v8, v4
	v_mul_lo_u32 v5, v5, s33
	v_lshlrev_b32_e32 v4, 4, v4
	v_add3_u32 v4, v135, v5, v4
	s_waitcnt vmcnt(19)
	ds_write_b128 v4, v[60:63]
	v_ashrrev_i32_e32 v4, 31, v6
	v_lshrrev_b32_e32 v4, 29, v4
	v_add_u32_e32 v4, v6, v4
	v_lshrrev_b32_e32 v5, 3, v4
	v_and_b32_e32 v4, 0xffffff8, v4
	v_sub_u32_e32 v4, v6, v4
	v_mul_lo_u32 v5, v5, s33
	v_lshlrev_b32_e32 v4, 4, v4
	s_or_b32 s39, s42, s39
	v_add3_u32 v4, v135, v5, v4
	s_or_b32 s80, s39, s41
	s_waitcnt vmcnt(18)
	ds_write_b128 v4, v[64:67]
	v_subrev_u32_e32 v4, s25, v8
	s_lshl_b64 s[42:43], s[80:81], 13
	s_lshl_b64 s[46:47], s[80:81], 14
	v_min_i32_e32 v4, 0xbf, v4
	s_add_u32 s50, s15, s46
	v_lshl_add_u32 v4, v4, 2, v136
	s_addc_u32 s51, s17, s47
	s_waitcnt vmcnt(17)
	ds_write_b32 v4, v137
	v_mov_b32_e32 v60, v176
	s_add_u32 s52, s13, s46
	s_waitcnt lgkmcnt(0)
	s_barrier
	s_addc_u32 s53, s14, s47
	v_add_u32_e32 v137, s11, v60
	s_add_u32 s54, s20, s46
	v_lshl_add_u32 v44, v60, 3, s9
	v_ashrrev_i32_e32 v60, 31, v137
	s_addc_u32 s55, s21, s47
	v_ashrrev_i32_e32 v45, 31, v44
	v_lshrrev_b32_e32 v60, 29, v60
	v_lshlrev_b64 v[4:5], 1, v[44:45]
	s_add_u32 s42, s18, s42
	v_subrev_u32_e32 v44, s10, v44
	v_add_u32_e32 v62, v137, v60
	s_addc_u32 s43, s19, s43
	v_ashrrev_i32_e32 v45, 31, v44
	v_lshlrev_b32_e32 v60, 4, v62
	v_and_b32_e32 v62, 0x1ffffff8, v62
	v_lshl_add_u64 v[44:45], v[44:45], 1, s[42:43]
	s_add_u32 s42, s2, s46
	v_and_b32_e32 v60, 0xffffff80, v60
	v_sub_u32_e32 v62, v137, v62
	v_lshl_add_u64 v[6:7], s[50:51], 0, v[4:5]
	v_lshl_add_u64 v[8:9], s[52:53], 0, v[4:5]
	v_lshl_add_u64 v[12:13], s[54:55], 0, v[4:5]
	s_addc_u32 s43, s3, s47
	v_ashrrev_i32_e32 v61, 31, v60
	v_lshlrev_b32_e32 v62, 3, v62
	global_load_dwordx4 v[40:43], v[6:7], off
	global_load_dwordx4 v[20:23], v[6:7], off offset:1024
	global_load_dwordx4 v[48:51], v[8:9], off
	global_load_dwordx4 v[24:27], v[8:9], off offset:1024
	global_load_dwordx4 v[56:59], v[12:13], off
	global_load_dwordx4 v[32:35], v[12:13], off offset:1024
	global_load_dwordx4 v[16:19], v[6:7], off offset:2048
	s_nop 0
	global_load_dwordx4 v[4:7], v[6:7], off offset:3072
	s_nop 0
	global_load_dwordx4 v[28:31], v[8:9], off offset:2048
	s_nop 0
	global_load_dwordx4 v[8:11], v[8:9], off offset:3072
	s_nop 0
	global_load_dwordx4 v[36:39], v[12:13], off offset:2048
	s_nop 0
	global_load_dwordx4 v[12:15], v[12:13], off offset:3072
	v_lshl_add_u64 v[60:61], v[60:61], 1, s[42:43]
	v_ashrrev_i32_e32 v63, 31, v62
	v_add_u32_e32 v64, 64, v137
	v_lshl_add_u64 v[60:61], v[62:63], 1, v[60:61]
	v_ashrrev_i32_e32 v62, 31, v64
	v_lshrrev_b32_e32 v62, 29, v62
	v_add_u32_e32 v65, v64, v62
	v_lshlrev_b32_e32 v62, 4, v65
	v_and_b32_e32 v62, 0xffffff80, v62
	v_and_b32_e32 v65, 0x1ffffff8, v65
	v_ashrrev_i32_e32 v63, 31, v62
	v_sub_u32_e32 v64, v64, v65
	v_subrev_u32_e32 v137, s25, v137
	s_mul_i32 s41, s80, 0x300
	v_lshl_add_u64 v[62:63], v[62:63], 1, s[42:43]
	v_lshlrev_b32_e32 v64, 3, v64
	v_min_i32_e32 v138, 0xbf, v137
	s_mul_hi_u32 s39, s80, 0x300
	s_add_u32 s42, s22, s41
	v_ashrrev_i32_e32 v65, 31, v64
	v_ashrrev_i32_e32 v139, 31, v138
	s_addc_u32 s43, s23, s39
	v_lshl_add_u64 v[64:65], v[64:65], 1, v[62:63]
	v_lshl_add_u64 v[138:139], v[138:139], 2, s[42:43]
	global_load_dwordx4 v[52:55], v[44:45], off
	s_nop 0
	global_load_dwordx4 v[44:47], v[44:45], off offset:1024
	s_nop 0
	global_load_dwordx4 v[60:63], v[60:61], off
	s_nop 0
	global_load_dwordx4 v[64:67], v[64:65], off
	v_mov_b32_e32 v137, v176
	global_load_dword v138, v[138:139], off
	s_nop 0
	v_lshlrev_b32_e32 v142, 4, v137
	v_add_u32_e32 v139, s35, v137
	v_and_b32_e32 v140, 0xf0, v142
	v_add_u32_e32 v140, v1, v140
	v_lshrrev_b32_e32 v143, 4, v139
	v_and_b32_e32 v142, 0x70, v142
	s_waitcnt vmcnt(17)
	v_mad_u64_u32 v[144:145], s[42:43], v143, s30, v[140:141]
	v_add_u32_e32 v142, v1, v142
	v_mbcnt_lo_u32_b32 v240, -1, 0
	v_mbcnt_hi_u32_b32 v240, -1, v240
	v_and_b32_e32 v240, 1, v240
	v_lshlrev_b32_e32 v240, 3, v240
	v_sub_u32_e32 v240, 0, v240
	v_add_u32_e32 v241, v144, v240
	ds_write2_b64 v241, v[112:113], v[114:115] offset1:2
	v_add_u32_e32 v242, 0x4400, v144
	v_add_u32_e32 v242, v242, v240
	ds_write2_b64 v242, v[120:121], v[122:123] offset1:2
	v_lshrrev_b32_e32 v112, 3, v139
	v_mad_u64_u32 v[112:113], s[42:43], v112, s33, v[142:143]
	v_add_u32_e32 v114, 64, v139
	v_add_u32_e32 v241, 0x8800, v112
	v_add_u32_e32 v241, v241, v240
	ds_write2_b64 v241, v[116:117], v[118:119] offset1:2
	v_lshrrev_b32_e32 v112, 4, v114
	v_mad_u64_u32 v[112:113], s[42:43], v112, s30, v[140:141]
	v_add_u32_e32 v242, v112, v240
	ds_write2_b64 v242, v[96:97], v[98:99] offset1:2
	v_add_u32_e32 v241, 0x4400, v112
	v_add_u32_e32 v241, v241, v240
	ds_write2_b64 v241, v[108:109], v[110:111] offset1:2
	v_lshrrev_b32_e32 v96, 3, v114
	v_mad_u64_u32 v[96:97], s[42:43], v96, s33, v[142:143]
	v_add_u32_e32 v98, 0x80, v139
	v_add_u32_e32 v242, 0x8800, v96
	v_add_u32_e32 v242, v242, v240
	ds_write2_b64 v242, v[100:101], v[102:103] offset1:2
	v_lshrrev_b32_e32 v96, 4, v98
	v_mad_u64_u32 v[96:97], s[42:43], v96, s30, v[140:141]
	v_add_u32_e32 v241, v96, v240
	ds_write2_b64 v241, v[84:85], v[86:87] offset1:2
	v_add_u32_e32 v242, 0x4400, v96
	v_add_u32_e32 v242, v242, v240
	ds_write2_b64 v242, v[104:105], v[106:107] offset1:2
	v_lshrrev_b32_e32 v84, 3, v98
	v_mad_u64_u32 v[84:85], s[42:43], v84, s33, v[142:143]
	v_add_u32_e32 v86, 0xc0, v139
	v_add_u32_e32 v241, 0x8800, v84
	v_add_u32_e32 v241, v241, v240
	ds_write2_b64 v241, v[92:93], v[94:95] offset1:2
	v_lshrrev_b32_e32 v84, 4, v86
	v_mad_u64_u32 v[84:85], s[42:43], v84, s30, v[140:141]
	v_add_u32_e32 v242, v84, v240
	ds_write2_b64 v242, v[68:69], v[70:71] offset1:2
	v_add_u32_e32 v241, 0x4400, v84
	v_add_u32_e32 v241, v241, v240
	ds_write2_b64 v241, v[76:77], v[78:79] offset1:2
	v_lshrrev_b32_e32 v68, 3, v86
	v_mad_u64_u32 v[68:69], s[42:43], v68, s33, v[142:143]
	v_add_u32_e32 v70, s11, v137
	v_add_u32_e32 v242, 0x8800, v68
	v_add_u32_e32 v242, v242, v240
	ds_write2_b64 v242, v[72:73], v[74:75] offset1:2
	v_lshrrev_b32_e32 v68, 3, v70
	v_mad_u64_u32 v[68:69], s[42:43], v68, s33, v[142:143]
	v_add_u32_e32 v71, 64, v70
	v_add_u32_e32 v241, 0xd000, v68
	v_add_u32_e32 v241, v241, v240
	ds_write2_b64 v241, v[88:89], v[90:91] offset1:2
	v_lshrrev_b32_e32 v68, 3, v71
	v_mad_u64_u32 v[68:69], s[42:43], v68, s33, v[142:143]
	v_add_u32_e32 v242, 0xd000, v68
	v_add_u32_e32 v242, v242, v240
	ds_write2_b64 v242, v[80:81], v[82:83] offset1:2
	v_ashrrev_i32_e32 v68, 31, v70
	v_lshrrev_b32_e32 v68, 29, v68
	v_add_u32_e32 v68, v70, v68
	v_lshrrev_b32_e32 v69, 3, v68
	v_and_b32_e32 v68, 0xffffff8, v68
	v_sub_u32_e32 v68, v70, v68
	v_mul_lo_u32 v69, v69, s33
	v_lshlrev_b32_e32 v68, 4, v68
	v_add3_u32 v68, v1, v69, v68
	ds_write_b128 v68, v[128:131] offset:63488
	v_ashrrev_i32_e32 v68, 31, v71
	v_lshrrev_b32_e32 v68, 29, v68
	v_add_u32_e32 v68, v71, v68
	v_lshrrev_b32_e32 v69, 3, v68
	v_and_b32_e32 v68, 0xffffff8, v68
	v_sub_u32_e32 v68, v71, v68
	v_mul_lo_u32 v69, v69, s33
	v_lshlrev_b32_e32 v68, 4, v68
	v_add3_u32 v68, v1, v69, v68
	ds_write_b128 v68, v[124:127] offset:63488
	v_subrev_u32_e32 v68, s25, v70
	v_min_i32_e32 v68, 0xbf, v68
	v_lshl_add_u32 v68, v68, 2, v1
	ds_write_b32 v68, v141 offset:62464
	s_waitcnt lgkmcnt(0)
	s_barrier
.LBB0_1640:
	s_add_i32 s39, s40, 2
	s_add_i32 s40, s40, 4
	s_min_u32 s40, s40, 0x43
	s_add_i32 s42, s40, -4
	s_sub_i32 s43, 0x43, s40
	s_and_b64 s[40:41], s[0:1], exec
	s_cselect_b32 s40, s42, s43
	s_add_i32 s40, s40, s38
	s_lshl_b32 s40, s40, 4
	s_or_b32 s80, s40, s8
	s_lshl_b64 s[40:41], s[80:81], 13
	s_lshl_b64 s[42:43], s[80:81], 14
	s_add_u32 s46, s15, s42
	s_addc_u32 s47, s17, s43
	s_add_u32 s50, s13, s42
	v_mov_b32_e32 v137, v176
	s_addc_u32 s51, s14, s43
	s_add_u32 s52, s20, s42
	v_lshl_add_u32 v68, v137, 3, s9
	s_addc_u32 s53, s21, s43
	v_ashrrev_i32_e32 v69, 31, v68
	v_lshlrev_b64 v[70:71], 1, v[68:69]
	s_add_u32 s40, s18, s40
	v_subrev_u32_e32 v68, s10, v68
	v_lshl_add_u64 v[72:73], s[46:47], 0, v[70:71]
	v_lshl_add_u64 v[74:75], s[50:51], 0, v[70:71]
	v_lshl_add_u64 v[70:71], s[52:53], 0, v[70:71]
	s_addc_u32 s41, s19, s41
	v_ashrrev_i32_e32 v69, 31, v68
	v_add_u32_e32 v137, s11, v137
	global_load_dwordx4 v[120:123], v[72:73], off
	global_load_dwordx4 v[128:131], v[74:75], off
	global_load_dwordx4 v[124:127], v[70:71], off
	global_load_dwordx4 v[112:115], v[72:73], off offset:1024
	global_load_dwordx4 v[116:119], v[74:75], off offset:1024
	global_load_dwordx4 v[108:111], v[70:71], off offset:1024
	global_load_dwordx4 v[100:103], v[72:73], off offset:2048
	global_load_dwordx4 v[104:107], v[74:75], off offset:2048
	global_load_dwordx4 v[96:99], v[70:71], off offset:2048
	global_load_dwordx4 v[88:91], v[72:73], off offset:3072
	global_load_dwordx4 v[92:95], v[74:75], off offset:3072
	global_load_dwordx4 v[84:87], v[70:71], off offset:3072
	v_lshl_add_u64 v[68:69], v[68:69], 1, s[40:41]
	v_add_u32_e32 v74, 64, v137
	global_load_dwordx4 v[80:83], v[68:69], off
	global_load_dwordx4 v[76:79], v[68:69], off offset:1024
	v_ashrrev_i32_e32 v68, 31, v137
	v_ashrrev_i32_e32 v72, 31, v74
	v_lshrrev_b32_e32 v68, 29, v68
	v_lshrrev_b32_e32 v72, 29, v72
	v_add_u32_e32 v70, v137, v68
	v_add_u32_e32 v75, v74, v72
	v_lshlrev_b32_e32 v68, 4, v70
	v_lshlrev_b32_e32 v72, 4, v75
	s_add_u32 s40, s2, s42
	v_and_b32_e32 v68, 0xffffff80, v68
	v_and_b32_e32 v72, 0xffffff80, v72
	s_addc_u32 s41, s3, s43
	v_ashrrev_i32_e32 v69, 31, v68
	v_and_b32_e32 v70, 0x1ffffff8, v70
	v_ashrrev_i32_e32 v73, 31, v72
	v_and_b32_e32 v75, 0x1ffffff8, v75
	v_lshl_add_u64 v[68:69], v[68:69], 1, s[40:41]
	v_sub_u32_e32 v70, v137, v70
	v_lshl_add_u64 v[72:73], v[72:73], 1, s[40:41]
	v_sub_u32_e32 v74, v74, v75
	v_subrev_u32_e32 v137, s25, v137
	s_mul_i32 s40, s80, 0x300
	v_lshlrev_b32_e32 v70, 3, v70
	v_lshlrev_b32_e32 v74, 3, v74
	v_min_i32_e32 v140, 0xbf, v137
	s_mul_hi_u32 s41, s80, 0x300
	s_add_u32 s40, s22, s40
	v_ashrrev_i32_e32 v71, 31, v70
	v_ashrrev_i32_e32 v75, 31, v74
	v_ashrrev_i32_e32 v141, 31, v140
	s_addc_u32 s41, s23, s41
	v_lshl_add_u64 v[68:69], v[70:71], 1, v[68:69]
	v_lshl_add_u64 v[72:73], v[74:75], 1, v[72:73]
	v_lshl_add_u64 v[140:141], v[140:141], 2, s[40:41]
	v_mov_b32_e32 v139, v176
	global_load_dwordx4 v[68:71], v[68:69], off
	s_nop 0
	global_load_dwordx4 v[72:75], v[72:73], off
	s_nop 0
	global_load_dword v137, v[140:141], off
	s_nop 0
	v_add_u32_e32 v141, s35, v139
	v_lshlrev_b32_e32 v140, 4, v139
	v_and_b32_e32 v142, 0xf0, v140
	v_lshrrev_b32_e32 v145, 4, v141
	v_add_u32_e32 v143, v2, v142
	v_mul_lo_u32 v145, v145, s30
	v_add_u32_e32 v142, v132, v142
	v_add_u32_e32 v146, v143, v145
	v_and_b32_e32 v144, 0x70, v140
	s_waitcnt vmcnt(33)
	v_mbcnt_lo_u32_b32 v240, -1, 0
	v_mbcnt_hi_u32_b32 v240, -1, v240
	v_and_b32_e32 v240, 1, v240
	v_lshlrev_b32_e32 v240, 3, v240
	v_sub_u32_e32 v240, 0, v240
	v_add_u32_e32 v241, v146, v240
	ds_write2_b64 v241, v[40:41], v[42:43] offset1:2
	v_add_u32_e32 v40, v142, v145
	v_add_u32_e32 v140, v133, v144
	s_waitcnt vmcnt(31)
	v_add_u32_e32 v242, v40, v240
	ds_write2_b64 v242, v[48:49], v[50:51] offset1:2
	v_lshrrev_b32_e32 v40, 3, v141
	v_mad_u64_u32 v[40:41], s[40:41], v40, s33, v[140:141]
	s_waitcnt vmcnt(29)
	v_add_u32_e32 v241, v40, v240
	ds_write2_b64 v241, v[56:57], v[58:59] offset1:2
	v_add_u32_e32 v40, 64, v141
	v_lshrrev_b32_e32 v41, 4, v40
	v_mul_lo_u32 v41, v41, s30
	v_add_u32_e32 v42, v143, v41
	v_add_u32_e32 v242, v42, v240
	ds_write2_b64 v242, v[20:21], v[22:23] offset1:2
	v_add_u32_e32 v20, v142, v41
	v_add_u32_e32 v241, v20, v240
	ds_write2_b64 v241, v[24:25], v[26:27] offset1:2
	v_lshrrev_b32_e32 v20, 3, v40
	v_mad_u64_u32 v[20:21], s[40:41], v20, s33, v[140:141]
	s_waitcnt vmcnt(28)
	v_add_u32_e32 v242, v20, v240
	ds_write2_b64 v242, v[32:33], v[34:35] offset1:2
	v_add_u32_e32 v20, 0x80, v141
	v_lshrrev_b32_e32 v21, 4, v20
	v_mul_lo_u32 v21, v21, s30
	v_add_u32_e32 v22, v143, v21
	s_waitcnt vmcnt(27)
	v_add_u32_e32 v241, v22, v240
	ds_write2_b64 v241, v[16:17], v[18:19] offset1:2
	v_add_u32_e32 v16, v142, v21
	s_waitcnt vmcnt(25)
	v_add_u32_e32 v242, v16, v240
	ds_write2_b64 v242, v[28:29], v[30:31] offset1:2
	v_lshrrev_b32_e32 v16, 3, v20
	v_mad_u64_u32 v[16:17], s[40:41], v16, s33, v[140:141]
	s_waitcnt vmcnt(23)
	v_add_u32_e32 v241, v16, v240
	ds_write2_b64 v241, v[36:37], v[38:39] offset1:2
	v_add_u32_e32 v16, 0xc0, v141
	v_lshrrev_b32_e32 v17, 4, v16
	v_mul_lo_u32 v17, v17, s30
	v_add_u32_e32 v18, v143, v17
	v_add_u32_e32 v242, v18, v240
	ds_write2_b64 v242, v[4:5], v[6:7] offset1:2
	v_add_u32_e32 v4, v142, v17
	v_add_u32_e32 v241, v4, v240
	ds_write2_b64 v241, v[8:9], v[10:11] offset1:2
	v_lshrrev_b32_e32 v4, 3, v16
	v_mad_u64_u32 v[4:5], s[40:41], v4, s33, v[140:141]
	v_add_u32_e32 v8, s11, v139
	s_waitcnt vmcnt(22)
	v_add_u32_e32 v242, v4, v240
	ds_write2_b64 v242, v[12:13], v[14:15] offset1:2
	v_add_u32_e32 v4, v134, v144
	v_lshrrev_b32_e32 v5, 3, v8
	v_mad_u64_u32 v[6:7], s[40:41], v5, s33, v[4:5]
	s_waitcnt vmcnt(21)
	v_add_u32_e32 v241, v6, v240
	ds_write2_b64 v241, v[52:53], v[54:55] offset1:2
	v_add_u32_e32 v6, 64, v8
	v_lshrrev_b32_e32 v5, 3, v6
	v_mad_u64_u32 v[4:5], s[40:41], v5, s33, v[4:5]
	s_waitcnt vmcnt(20)
	v_add_u32_e32 v242, v4, v240
	ds_write2_b64 v242, v[44:45], v[46:47] offset1:2
	v_ashrrev_i32_e32 v4, 31, v8
	v_lshrrev_b32_e32 v4, 29, v4
	v_add_u32_e32 v4, v8, v4
	v_lshrrev_b32_e32 v5, 3, v4
	v_and_b32_e32 v4, 0xffffff8, v4
	v_sub_u32_e32 v4, v8, v4
	v_mul_lo_u32 v5, v5, s33
	v_lshlrev_b32_e32 v4, 4, v4
	v_add3_u32 v4, v135, v5, v4
	s_waitcnt vmcnt(19)
	ds_write_b128 v4, v[60:63]
	v_ashrrev_i32_e32 v4, 31, v6
	s_min_u32 s40, s39, 64
	v_lshrrev_b32_e32 v4, 29, v4
	s_add_i32 s42, s40, -1
	s_sub_i32 s43, 64, s40
	v_add_u32_e32 v4, v6, v4
	s_and_b64 s[40:41], s[0:1], exec
	v_lshrrev_b32_e32 v5, 3, v4
	v_and_b32_e32 v4, 0xffffff8, v4
	s_cselect_b32 s40, s42, s43
	v_sub_u32_e32 v4, v6, v4
	s_add_i32 s40, s40, s38
	v_mul_lo_u32 v5, v5, s33
	v_lshlrev_b32_e32 v4, 4, v4
	s_lshl_b32 s40, s40, 4
	v_add3_u32 v4, v135, v5, v4
	s_or_b32 s80, s40, s8
	s_waitcnt vmcnt(18)
	ds_write_b128 v4, v[64:67]
	v_subrev_u32_e32 v4, s25, v8
	s_lshl_b64 s[40:41], s[80:81], 13
	s_lshl_b64 s[42:43], s[80:81], 14
	v_min_i32_e32 v4, 0xbf, v4
	s_add_u32 s46, s15, s42
	v_lshl_add_u32 v4, v4, 2, v136
	s_addc_u32 s47, s17, s43
	s_waitcnt vmcnt(17)
	ds_write_b32 v4, v138
	v_mov_b32_e32 v60, v176
	s_add_u32 s50, s13, s42
	s_waitcnt lgkmcnt(0)
	s_barrier
	s_addc_u32 s51, s14, s43
	v_lshl_add_u32 v44, v60, 3, s9
	v_add_u32_e32 v138, s11, v60
	s_add_u32 s52, s20, s42
	v_ashrrev_i32_e32 v45, 31, v44
	v_add_u32_e32 v66, 64, v138
	s_addc_u32 s53, s21, s43
	v_lshlrev_b64 v[4:5], 1, v[44:45]
	v_ashrrev_i32_e32 v60, 31, v138
	v_ashrrev_i32_e32 v64, 31, v66
	v_lshl_add_u64 v[6:7], s[46:47], 0, v[4:5]
	v_lshl_add_u64 v[8:9], s[50:51], 0, v[4:5]
	v_lshl_add_u64 v[12:13], s[52:53], 0, v[4:5]
	v_lshrrev_b32_e32 v60, 29, v60
	v_lshrrev_b32_e32 v64, 29, v64
	global_load_dwordx4 v[40:43], v[6:7], off
	global_load_dwordx4 v[48:51], v[8:9], off
	global_load_dwordx4 v[56:59], v[12:13], off
	global_load_dwordx4 v[20:23], v[6:7], off offset:1024
	global_load_dwordx4 v[24:27], v[8:9], off offset:1024
	global_load_dwordx4 v[32:35], v[12:13], off offset:1024
	global_load_dwordx4 v[16:19], v[6:7], off offset:2048
	global_load_dwordx4 v[28:31], v[8:9], off offset:2048
	global_load_dwordx4 v[36:39], v[12:13], off offset:2048
	s_nop 0
	global_load_dwordx4 v[4:7], v[6:7], off offset:3072
	s_nop 0
	global_load_dwordx4 v[8:11], v[8:9], off offset:3072
	s_nop 0
	global_load_dwordx4 v[12:15], v[12:13], off offset:3072
	s_add_u32 s40, s18, s40
	v_subrev_u32_e32 v44, s10, v44
	v_add_u32_e32 v62, v138, v60
	v_add_u32_e32 v67, v66, v64
	s_addc_u32 s41, s19, s41
	v_ashrrev_i32_e32 v45, 31, v44
	v_lshlrev_b32_e32 v60, 4, v62
	v_lshlrev_b32_e32 v64, 4, v67
	v_lshl_add_u64 v[44:45], v[44:45], 1, s[40:41]
	s_add_u32 s40, s2, s42
	v_and_b32_e32 v60, 0xffffff80, v60
	v_and_b32_e32 v64, 0xffffff80, v64
	s_addc_u32 s41, s3, s43
	v_ashrrev_i32_e32 v61, 31, v60
	v_and_b32_e32 v62, 0x1ffffff8, v62
	v_ashrrev_i32_e32 v65, 31, v64
	v_and_b32_e32 v67, 0x1ffffff8, v67
	v_lshl_add_u64 v[60:61], v[60:61], 1, s[40:41]
	v_sub_u32_e32 v62, v138, v62
	v_lshl_add_u64 v[64:65], v[64:65], 1, s[40:41]
	v_sub_u32_e32 v66, v66, v67
	v_subrev_u32_e32 v138, s25, v138
	s_mul_i32 s40, s80, 0x300
	v_lshlrev_b32_e32 v62, 3, v62
	v_lshlrev_b32_e32 v66, 3, v66
	v_min_i32_e32 v138, 0xbf, v138
	s_mul_hi_u32 s41, s80, 0x300
	s_add_u32 s40, s22, s40
	v_ashrrev_i32_e32 v63, 31, v62
	v_ashrrev_i32_e32 v67, 31, v66
	v_ashrrev_i32_e32 v139, 31, v138
	s_addc_u32 s41, s23, s41
	v_lshl_add_u64 v[60:61], v[62:63], 1, v[60:61]
	v_lshl_add_u64 v[64:65], v[66:67], 1, v[64:65]
	v_lshl_add_u64 v[138:139], v[138:139], 2, s[40:41]
	global_load_dwordx4 v[52:55], v[44:45], off
	s_nop 0
	global_load_dwordx4 v[44:47], v[44:45], off offset:1024
	s_cmpk_gt_u32 s39, 0x41
	global_load_dwordx4 v[60:63], v[60:61], off
	s_nop 0
	global_load_dwordx4 v[64:67], v[64:65], off
	s_nop 0
	global_load_dword v138, v[138:139], off
	v_mov_b32_e32 v139, v176
	s_nop 0
	v_lshlrev_b32_e32 v142, 4, v139
	v_add_u32_e32 v141, s35, v139
	v_and_b32_e32 v140, 0xf0, v142
	v_add_u32_e32 v140, v1, v140
	v_lshrrev_b32_e32 v143, 4, v141
	v_and_b32_e32 v142, 0x70, v142
	v_mad_u64_u32 v[144:145], s[40:41], v143, s30, v[140:141]
	v_add_u32_e32 v142, v1, v142
	s_waitcnt vmcnt(33)
	v_mbcnt_lo_u32_b32 v240, -1, 0
	v_mbcnt_hi_u32_b32 v240, -1, v240
	v_and_b32_e32 v240, 1, v240
	v_lshlrev_b32_e32 v240, 3, v240
	v_sub_u32_e32 v240, 0, v240
	v_add_u32_e32 v241, v144, v240
	ds_write2_b64 v241, v[120:121], v[122:123] offset1:2
	s_waitcnt vmcnt(32)
	v_add_u32_e32 v242, 0x4400, v144
	v_add_u32_e32 v242, v242, v240
	ds_write2_b64 v242, v[128:129], v[130:131] offset1:2
	v_lshrrev_b32_e32 v120, 3, v141
	v_mad_u64_u32 v[120:121], s[40:41], v120, s33, v[142:143]
	v_add_u32_e32 v122, 64, v141
	s_waitcnt vmcnt(31)
	v_add_u32_e32 v241, 0x8800, v120
	v_add_u32_e32 v241, v241, v240
	ds_write2_b64 v241, v[124:125], v[126:127] offset1:2
	v_lshrrev_b32_e32 v120, 4, v122
	v_mad_u64_u32 v[120:121], s[40:41], v120, s30, v[140:141]
	s_waitcnt vmcnt(30)
	v_add_u32_e32 v242, v120, v240
	ds_write2_b64 v242, v[112:113], v[114:115] offset1:2
	s_waitcnt vmcnt(29)
	v_add_u32_e32 v241, 0x4400, v120
	v_add_u32_e32 v241, v241, v240
	ds_write2_b64 v241, v[116:117], v[118:119] offset1:2
	v_lshrrev_b32_e32 v112, 3, v122
	v_mad_u64_u32 v[112:113], s[40:41], v112, s33, v[142:143]
	s_waitcnt vmcnt(28)
	v_add_u32_e32 v242, 0x8800, v112
	v_add_u32_e32 v242, v242, v240
	ds_write2_b64 v242, v[108:109], v[110:111] offset1:2
	v_add_u32_e32 v110, 0x80, v141
	v_lshrrev_b32_e32 v108, 4, v110
	v_mad_u64_u32 v[108:109], s[40:41], v108, s30, v[140:141]
	s_waitcnt vmcnt(27)
	v_add_u32_e32 v241, v108, v240
	ds_write2_b64 v241, v[100:101], v[102:103] offset1:2
	s_waitcnt vmcnt(26)
	v_add_u32_e32 v242, 0x4400, v108
	v_add_u32_e32 v242, v242, v240
	ds_write2_b64 v242, v[104:105], v[106:107] offset1:2
	v_lshrrev_b32_e32 v100, 3, v110
	v_mad_u64_u32 v[100:101], s[40:41], v100, s33, v[142:143]
	s_waitcnt vmcnt(25)
	v_add_u32_e32 v241, 0x8800, v100
	v_add_u32_e32 v241, v241, v240
	ds_write2_b64 v241, v[96:97], v[98:99] offset1:2
	v_add_u32_e32 v98, 0xc0, v141
	v_lshrrev_b32_e32 v96, 4, v98
	v_mad_u64_u32 v[96:97], s[40:41], v96, s30, v[140:141]
	s_waitcnt vmcnt(24)
	v_add_u32_e32 v242, v96, v240
	ds_write2_b64 v242, v[88:89], v[90:91] offset1:2
	s_waitcnt vmcnt(23)
	v_add_u32_e32 v241, 0x4400, v96
	v_add_u32_e32 v241, v241, v240
	ds_write2_b64 v241, v[92:93], v[94:95] offset1:2
	v_lshrrev_b32_e32 v88, 3, v98
	v_mad_u64_u32 v[88:89], s[40:41], v88, s33, v[142:143]
	s_waitcnt vmcnt(22)
	v_add_u32_e32 v242, 0x8800, v88
	v_add_u32_e32 v242, v242, v240
	ds_write2_b64 v242, v[84:85], v[86:87] offset1:2
	v_add_u32_e32 v86, s11, v139
	v_lshrrev_b32_e32 v84, 3, v86
	v_mad_u64_u32 v[84:85], s[40:41], v84, s33, v[142:143]
	s_waitcnt vmcnt(21)
	v_add_u32_e32 v241, 0xd000, v84
	v_add_u32_e32 v241, v241, v240
	ds_write2_b64 v241, v[80:81], v[82:83] offset1:2
	v_add_u32_e32 v82, 64, v86
	v_lshrrev_b32_e32 v80, 3, v82
	v_mad_u64_u32 v[80:81], s[40:41], v80, s33, v[142:143]
	s_waitcnt vmcnt(20)
	v_add_u32_e32 v242, 0xd000, v80
	v_add_u32_e32 v242, v242, v240
	ds_write2_b64 v242, v[76:77], v[78:79] offset1:2
	v_ashrrev_i32_e32 v76, 31, v86
	v_lshrrev_b32_e32 v76, 29, v76
	v_add_u32_e32 v76, v86, v76
	v_lshrrev_b32_e32 v77, 3, v76
	v_and_b32_e32 v76, 0xffffff8, v76
	v_sub_u32_e32 v76, v86, v76
	v_mul_lo_u32 v77, v77, s33
	v_lshlrev_b32_e32 v76, 4, v76
	v_add3_u32 v76, v1, v77, v76
	s_waitcnt vmcnt(19)
	ds_write_b128 v76, v[68:71] offset:63488
	v_ashrrev_i32_e32 v68, 31, v82
	v_lshrrev_b32_e32 v68, 29, v68
	v_add_u32_e32 v68, v82, v68
	v_lshrrev_b32_e32 v69, 3, v68
	v_and_b32_e32 v68, 0xffffff8, v68
	v_sub_u32_e32 v68, v82, v68
	v_mul_lo_u32 v69, v69, s33
	v_lshlrev_b32_e32 v68, 4, v68
	v_add3_u32 v68, v1, v69, v68
	s_waitcnt vmcnt(18)
	ds_write_b128 v68, v[72:75] offset:63488
	v_subrev_u32_e32 v68, s25, v86
	v_min_i32_e32 v68, 0xbf, v68
	v_lshl_add_u32 v68, v68, 2, v1
	s_waitcnt vmcnt(17)
	ds_write_b32 v68, v137 offset:62464
	s_waitcnt lgkmcnt(0)
	s_barrier
	s_mov_b32 s40, s39
	s_cbranch_scc0 .LBB0_1640
	v_mov_b32_e32 v134, 0x3ecc95a3
	s_branch .LBB0_1626
